# NA: skip QK/softmax/PV for key rows outside the wave window (exact zeros), incl. peeled last tile
# speedup vs baseline: 1.0426x; 1.0054x over previous
.LBB0_469:
	v_lshl_add_u64 v[66:67], v[154:155], 0, s[96:97]
	v_add_co_u32_e32 v70, vcc, 0x52002000, v66
	v_lshl_add_u64 v[68:69], v[156:157], 0, s[96:97]
	s_nop 0
	v_addc_co_u32_e32 v71, vcc, 0, v67, vcc
	global_load_dwordx2 v[164:165], v[70:71], off
	v_add_co_u32_e32 v70, vcc, 0x52002000, v68
	s_and_b32 s1, s3, 0x4000
	s_nop 0
	v_addc_co_u32_e32 v71, vcc, 0, v69, vcc
	v_add_co_u32_e32 v66, vcc, 0x4e002000, v66
	global_load_dwordx2 v[162:163], v[70:71], off
	s_nop 0
	v_addc_co_u32_e32 v67, vcc, 0, v67, vcc
	global_load_dwordx2 v[160:161], v[66:67], off
	v_add_co_u32_e32 v66, vcc, 0x4e002000, v68
	s_add_i32 s72, s1, 0
	s_nop 0
	v_addc_co_u32_e32 v67, vcc, 0, v69, vcc
	v_add3_u32 v0, s72, v199, v189
	v_add3_u32 v98, s72, v197, v189
	global_load_dwordx2 v[158:159], v[66:67], off
	s_cmp_lt_u32 s92, s84
	s_cbranch_scc1 .Lna_skip
	s_cmp_ge_u32 s92, s88
	s_cbranch_scc1 .Lna_skip
	ds_read_b128 v[66:69], v0 offset:32768
	ds_read_b128 v[98:101], v98 offset:32768
	v_add_u32_e32 v0, s72, v189
	v_add_u32_e32 v70, v0, v199
	ds_read_b128 v[70:73], v70 offset:40960
	v_add_u32_e32 v102, v0, v197
	ds_read_b128 v[102:105], v102 offset:40960
	s_waitcnt lgkmcnt(3)
	v_mfma_f32_32x32x16_bf16 v[82:97], v[66:69], v[114:117], 0
	s_cmp_lt_u32 s92, s84
	s_waitcnt lgkmcnt(1)
	v_mfma_f32_32x32x16_bf16 v[66:81], v[70:73], v[114:117], 0
	s_waitcnt lgkmcnt(0)
	v_mfma_f32_32x32x16_bf16 v[66:81], v[102:105], v[118:121], v[66:81]
	v_add_u32_e32 v102, v0, v195
	ds_read_b128 v[102:105], v102 offset:40960
	s_waitcnt lgkmcnt(0)
	v_mfma_f32_32x32x16_bf16 v[66:81], v[102:105], v[122:125], v[66:81]
	v_add_u32_e32 v102, v0, v194
	ds_read_b128 v[102:105], v102 offset:40960
	s_waitcnt lgkmcnt(0)
	v_mfma_f32_32x32x16_bf16 v[66:81], v[102:105], v[126:129], v[66:81]
	v_add_u32_e32 v102, v0, v193
	ds_read_b128 v[102:105], v102 offset:40960
	s_waitcnt lgkmcnt(0)
	v_mfma_f32_32x32x16_bf16 v[66:81], v[102:105], v[130:133], v[66:81]
	v_add_u32_e32 v102, v0, v192
	ds_read_b128 v[102:105], v102 offset:40960
	v_mfma_f32_32x32x16_bf16 v[82:97], v[98:101], v[118:121], v[82:97]
	v_add3_u32 v98, s72, v195, v189
	ds_read_b128 v[98:101], v98 offset:32768
	s_waitcnt lgkmcnt(1)
	v_mfma_f32_32x32x16_bf16 v[66:81], v[102:105], v[134:137], v[66:81]
	v_add_u32_e32 v102, v0, v191
	ds_read_b128 v[102:105], v102 offset:40960
	v_add_u32_e32 v0, v0, v190
	s_waitcnt lgkmcnt(0)
	v_mfma_f32_32x32x16_bf16 v[66:81], v[102:105], v[138:141], v[66:81]
	ds_read_b128 v[102:105], v0 offset:40960
	v_mfma_f32_32x32x16_bf16 v[82:97], v[98:101], v[122:125], v[82:97]
	v_add3_u32 v98, s72, v194, v189
	ds_read_b128 v[98:101], v98 offset:32768
	s_waitcnt lgkmcnt(0)
	v_mfma_f32_32x32x16_bf16 v[82:97], v[98:101], v[126:129], v[82:97]
	v_add3_u32 v98, s72, v193, v189
	ds_read_b128 v[98:101], v98 offset:32768
	s_waitcnt lgkmcnt(0)
	v_mfma_f32_32x32x16_bf16 v[82:97], v[98:101], v[130:133], v[82:97]
	v_add3_u32 v98, s72, v192, v189
	ds_read_b128 v[98:101], v98 offset:32768
	s_waitcnt lgkmcnt(0)
	v_mfma_f32_32x32x16_bf16 v[82:97], v[98:101], v[134:137], v[82:97]
	v_add3_u32 v98, s72, v191, v189
	ds_read_b128 v[98:101], v98 offset:32768
	s_waitcnt lgkmcnt(0)
	v_mfma_f32_32x32x16_bf16 v[82:97], v[98:101], v[138:141], v[82:97]
	v_add3_u32 v98, s72, v190, v189
	ds_read_b128 v[98:101], v98 offset:32768
	s_cselect_b64 s[72:73], -1, 0
	s_cmp_ge_u32 s92, s88
	s_cselect_b64 s[86:87], -1, 0
	s_or_b64 s[86:87], s[72:73], s[86:87]
	s_mov_b64 s[72:73], -1
	s_waitcnt lgkmcnt(0)
	s_add_i32 s72, s2, s92
	v_med3_i32 v239, s72, -7, 7
	v_lshlrev_b32_e32 v239, 7, v239
	v_lshl_add_u32 v239, v183, 2, v239
	v_add_u32_e32 v239, 0x10bbc, v239
	ds_read2_b32 v[206:207], v239 offset0:0 offset1:32
	ds_read2_b32 v[208:209], v239 offset0:1 offset1:33
	ds_read2_b32 v[210:211], v239 offset0:2 offset1:34
	ds_read2_b32 v[212:213], v239 offset0:3 offset1:35
	ds_read2_b32 v[214:215], v239 offset0:8 offset1:40
	ds_read2_b32 v[216:217], v239 offset0:9 offset1:41
	ds_read2_b32 v[218:219], v239 offset0:10 offset1:42
	ds_read2_b32 v[220:221], v239 offset0:11 offset1:43
	ds_read2_b32 v[222:223], v239 offset0:16 offset1:48
	ds_read2_b32 v[224:225], v239 offset0:17 offset1:49
	ds_read2_b32 v[226:227], v239 offset0:18 offset1:50
	ds_read2_b32 v[228:229], v239 offset0:19 offset1:51
	ds_read2_b32 v[230:231], v239 offset0:24 offset1:56
	ds_read2_b32 v[232:233], v239 offset0:25 offset1:57
	ds_read2_b32 v[234:235], v239 offset0:26 offset1:58
	ds_read2_b32 v[236:237], v239 offset0:27 offset1:59
	v_mfma_f32_32x32x16_bf16 v[82:97], v[98:101], v[142:145], v[82:97]
	s_and_b64 vcc, exec, s[86:87]
	v_mfma_f32_32x32x16_bf16 v[66:81], v[102:105], v[142:145], v[66:81]
	v_mov_b32_e32 v238, 0xff800000
	s_nop 11
	s_cbranch_vccnz .Lna_inv
	s_waitcnt lgkmcnt(0)
	v_add_f32_e32 v206, v82, v206
	v_add_f32_e32 v207, v66, v207
	v_cndmask_b32_e64 v82, v238, v206, s[70:71]
	v_cndmask_b32_e64 v0, v238, v207, s[68:69]
	v_add_f32_e32 v208, v83, v208
	v_add_f32_e32 v209, v67, v209
	v_cndmask_b32_e64 v83, v238, v208, s[66:67]
	v_cndmask_b32_e64 v66, v238, v209, s[64:65]
	v_add_f32_e32 v210, v84, v210
	v_add_f32_e32 v211, v68, v211
	v_cndmask_b32_e64 v84, v238, v210, s[62:63]
	v_cndmask_b32_e64 v67, v238, v211, s[60:61]
	v_add_f32_e32 v212, v85, v212
	v_add_f32_e32 v213, v69, v213
	v_cndmask_b32_e64 v85, v238, v212, s[58:59]
	v_cndmask_b32_e64 v68, v238, v213, s[56:57]
	v_add_f32_e32 v214, v86, v214
	v_add_f32_e32 v215, v70, v215
	v_cndmask_b32_e64 v86, v238, v214, s[54:55]
	v_cndmask_b32_e64 v69, v238, v215, s[52:53]
	v_add_f32_e32 v216, v87, v216
	v_add_f32_e32 v217, v71, v217
	v_cndmask_b32_e64 v87, v238, v216, s[50:51]
	v_cndmask_b32_e64 v70, v238, v217, s[48:49]
	v_add_f32_e32 v218, v88, v218
	v_add_f32_e32 v219, v72, v219
	v_cndmask_b32_e64 v88, v238, v218, s[46:47]
	v_cndmask_b32_e64 v71, v238, v219, s[44:45]
	v_add_f32_e32 v220, v89, v220
	v_add_f32_e32 v221, v73, v221
	v_cndmask_b32_e64 v89, v238, v220, s[42:43]
	v_cndmask_b32_e64 v72, v238, v221, s[40:41]
	v_add_f32_e32 v222, v90, v222
	v_add_f32_e32 v223, v74, v223
	v_cndmask_b32_e64 v90, v238, v222, s[38:39]
	v_cndmask_b32_e64 v73, v238, v223, s[36:37]
	v_add_f32_e32 v224, v91, v224
	v_add_f32_e32 v225, v75, v225
	v_cndmask_b32_e64 v91, v238, v224, s[34:35]
	v_cndmask_b32_e64 v74, v238, v225, s[30:31]
	v_add_f32_e32 v226, v92, v226
	v_add_f32_e32 v227, v76, v227
	v_cndmask_b32_e64 v92, v238, v226, s[28:29]
	v_cndmask_b32_e64 v75, v238, v227, s[26:27]
	v_add_f32_e32 v228, v93, v228
	v_add_f32_e32 v229, v77, v229
	v_cndmask_b32_e64 v93, v238, v228, s[24:25]
	v_cndmask_b32_e64 v76, v238, v229, s[22:23]
	v_add_f32_e32 v230, v94, v230
	v_add_f32_e32 v231, v78, v231
	v_cndmask_b32_e64 v94, v238, v230, s[20:21]
	v_cndmask_b32_e64 v77, v238, v231, s[18:19]
	v_add_f32_e32 v232, v95, v232
	v_add_f32_e32 v233, v79, v233
	v_cndmask_b32_e64 v95, v238, v232, s[16:17]
	v_cndmask_b32_e64 v78, v238, v233, s[14:15]
	v_add_f32_e32 v234, v96, v234
	v_add_f32_e32 v235, v80, v235
	v_cndmask_b32_e64 v96, v238, v234, s[12:13]
	v_cndmask_b32_e64 v79, v238, v235, s[10:11]
	v_add_f32_e32 v236, v97, v236
	v_add_f32_e32 v237, v81, v237
	v_cndmask_b32_e64 v97, v238, v236, s[8:9]
	v_cndmask_b32_e64 v80, v238, v237, s[6:7]
	s_branch .LBB0_597

.Lna_skip:
	s_waitcnt vmcnt(3)
	v_cvt_f32_fp8_e32 v66, v164
	v_cvt_f32_fp8_sdwa v67, v164 src0_sel:BYTE_1
	s_waitcnt vmcnt(0)
	v_cvt_pk_bf16_f32 v66, v66, v67
	v_cvt_f32_fp8_sdwa v67, v164 src0_sel:BYTE_2
	v_cvt_f32_fp8_sdwa v68, v164 src0_sel:BYTE_3
	v_cvt_pk_bf16_f32 v67, v67, v68
	v_cvt_f32_fp8_e32 v68, v165
	v_cvt_f32_fp8_sdwa v69, v165 src0_sel:BYTE_1
	v_cvt_pk_bf16_f32 v68, v68, v69
	v_cvt_f32_fp8_sdwa v69, v165 src0_sel:BYTE_2
	v_cvt_f32_fp8_sdwa v70, v165 src0_sel:BYTE_3
	v_cvt_pk_bf16_f32 v69, v69, v70
	s_waitcnt vmcnt(2)
	v_cvt_f32_fp8_e32 v70, v162
	v_cvt_f32_fp8_sdwa v71, v162 src0_sel:BYTE_1
	v_cvt_pk_bf16_f32 v70, v70, v71
	v_cvt_f32_fp8_sdwa v71, v162 src0_sel:BYTE_2
	v_cvt_f32_fp8_sdwa v72, v162 src0_sel:BYTE_3
	v_cvt_pk_bf16_f32 v71, v71, v72
	v_cvt_f32_fp8_e32 v72, v163
	v_cvt_f32_fp8_sdwa v73, v163 src0_sel:BYTE_1
	v_cvt_pk_bf16_f32 v72, v72, v73
	v_cvt_f32_fp8_sdwa v73, v163 src0_sel:BYTE_2
	v_cvt_f32_fp8_sdwa v74, v163 src0_sel:BYTE_3
	v_cvt_pk_bf16_f32 v73, v73, v74
	s_waitcnt vmcnt(1)
	v_cvt_f32_fp8_e32 v74, v160
	v_cvt_f32_fp8_sdwa v75, v160 src0_sel:BYTE_1
	v_cvt_pk_bf16_f32 v74, v74, v75
	v_cvt_f32_fp8_sdwa v75, v160 src0_sel:BYTE_2
	v_cvt_f32_fp8_sdwa v76, v160 src0_sel:BYTE_3
	v_cvt_pk_bf16_f32 v75, v75, v76
	v_cvt_f32_fp8_e32 v76, v161
	v_cvt_f32_fp8_sdwa v77, v161 src0_sel:BYTE_1
	v_cvt_pk_bf16_f32 v76, v76, v77
	v_cvt_f32_fp8_sdwa v77, v161 src0_sel:BYTE_2
	v_cvt_f32_fp8_sdwa v78, v161 src0_sel:BYTE_3
	v_cvt_pk_bf16_f32 v77, v77, v78
	s_waitcnt vmcnt(0)
	v_cvt_f32_fp8_e32 v78, v158
	v_cvt_f32_fp8_sdwa v79, v158 src0_sel:BYTE_1
	v_cvt_pk_bf16_f32 v78, v78, v79
	v_cvt_f32_fp8_sdwa v79, v158 src0_sel:BYTE_2
	v_cvt_f32_fp8_sdwa v80, v158 src0_sel:BYTE_3
	v_cvt_pk_bf16_f32 v79, v79, v80
	v_cvt_f32_fp8_e32 v80, v159
	v_cvt_f32_fp8_sdwa v81, v159 src0_sel:BYTE_1
	v_cvt_pk_bf16_f32 v80, v80, v81
	v_cvt_f32_fp8_sdwa v81, v159 src0_sel:BYTE_2
	v_cvt_f32_fp8_sdwa v82, v159 src0_sel:BYTE_3
	v_cvt_pk_bf16_f32 v81, v81, v82
	v_lshlrev_b32_e32 v82, 16, v74
	v_and_b32_e32 v74, 0xffff0000, v74
	v_lshlrev_b32_e32 v83, 16, v75
	v_and_b32_e32 v75, 0xffff0000, v75
	v_mul_f32_e32 v86, v74, v74
	v_mul_f32_e32 v87, v75, v75
	v_lshlrev_b32_e32 v84, 16, v76
	v_and_b32_e32 v76, 0xffff0000, v76
	v_fmac_f32_e32 v86, v82, v82
	v_fmac_f32_e32 v87, v83, v83
	v_add_f32_e32 v86, v86, v87
	v_mul_f32_e32 v87, v76, v76
	v_lshlrev_b32_e32 v85, 16, v77
	v_and_b32_e32 v77, 0xffff0000, v77
	v_fmac_f32_e32 v87, v84, v84
	v_add_f32_e32 v86, v86, v87
	v_mul_f32_e32 v87, v77, v77
	v_fmac_f32_e32 v87, v85, v85
	v_add_f32_e32 v86, v86, v87
	ds_bpermute_b32 v87, v185, v86
	s_xor_b32 s1, s1, 0x4000
	s_add_i32 s1, s1, 0
	s_add_i32 s92, s92, 1
	s_addk_i32 s3, 0x4000
	s_waitcnt lgkmcnt(0)
	v_add_f32_e32 v86, v86, v87
	ds_bpermute_b32 v87, v186, v86
	s_add_u32 s96, s96, 0x2000
	s_addc_u32 s97, s97, 0
	s_cmp_eq_u32 s96, 0x16000
	s_waitcnt lgkmcnt(0)
	v_add_f32_e32 v86, v86, v87
	ds_bpermute_b32 v87, v187, v86
	s_waitcnt lgkmcnt(0)
	v_add_f32_e32 v86, v86, v87
	ds_bpermute_b32 v87, v188, v86
	s_waitcnt lgkmcnt(0)
	v_add_f32_e32 v86, v86, v87
	v_fmamk_f32 v86, v86, 0x3c000000, v167
	v_cmp_gt_f32_e32 vcc, s81, v86
	v_mul_f32_e32 v87, 0x4f800000, v86
	s_nop 0
	v_cndmask_b32_e32 v86, v86, v87, vcc
	v_sqrt_f32_e32 v87, v86
	s_nop 0
	v_add_u32_e32 v88, -1, v87
	v_fma_f32 v89, -v88, v87, v86
	v_cmp_ge_f32_e64 s[72:73], 0, v89
	v_add_u32_e32 v89, 1, v87
	s_nop 0
	v_cndmask_b32_e64 v88, v87, v88, s[72:73]
	v_fma_f32 v87, -v89, v87, v86
	v_cmp_lt_f32_e64 s[72:73], 0, v87
	s_nop 1
	v_cndmask_b32_e64 v87, v88, v89, s[72:73]
	v_mul_f32_e32 v88, 0x37800000, v87
	v_cndmask_b32_e32 v87, v87, v88, vcc
	v_cmp_class_f32_e32 vcc, v86, v168
	s_nop 1
	v_cndmask_b32_e32 v86, v87, v86, vcc
	v_div_scale_f32 v87, s[72:73], v86, v86, 1.0
	v_rcp_f32_e32 v88, v87
	s_nop 0
	v_fma_f32 v89, -v87, v88, 1.0
	v_fmac_f32_e32 v88, v89, v88
	v_div_scale_f32 v89, vcc, 1.0, v86, 1.0
	v_mul_f32_e32 v90, v89, v88
	v_fma_f32 v91, -v87, v90, v89
	v_fmac_f32_e32 v90, v91, v88
	v_fma_f32 v87, -v87, v90, v89
	v_div_fmas_f32 v87, v87, v88, v90
	v_div_fixup_f32 v86, v87, v86, 1.0
	v_mul_f32_e32 v82, v86, v82
	v_mul_f32_e32 v74, v86, v74
	v_mul_f32_e32 v82, v150, v82
	v_mul_f32_e32 v74, v151, v74
	v_cvt_pk_bf16_f32 v74, v82, v74
	v_mul_f32_e32 v82, v86, v83
	v_mul_f32_e32 v75, v86, v75
	v_mul_f32_e32 v82, v152, v82
	v_mul_f32_e32 v75, v153, v75
	v_cvt_pk_bf16_f32 v75, v82, v75
	v_mul_f32_e32 v82, v86, v84
	v_mul_f32_e32 v76, v86, v76
	v_mul_f32_e32 v82, v146, v82
	v_mul_f32_e32 v76, v147, v76
	v_cvt_pk_bf16_f32 v76, v82, v76
	v_mul_f32_e32 v82, v86, v85
	v_mul_f32_e32 v77, v86, v77
	v_mul_f32_e32 v82, v148, v82
	v_mul_f32_e32 v77, v149, v77
	v_cvt_pk_bf16_f32 v77, v82, v77
	v_lshlrev_b32_e32 v82, 16, v78
	v_and_b32_e32 v78, 0xffff0000, v78
	v_lshlrev_b32_e32 v83, 16, v79
	v_and_b32_e32 v79, 0xffff0000, v79
	v_mul_f32_e32 v86, v78, v78
	v_mul_f32_e32 v87, v79, v79
	v_lshlrev_b32_e32 v84, 16, v80
	v_and_b32_e32 v80, 0xffff0000, v80
	v_fmac_f32_e32 v86, v82, v82
	v_fmac_f32_e32 v87, v83, v83
	v_add_f32_e32 v86, v86, v87
	v_mul_f32_e32 v87, v80, v80
	v_lshlrev_b32_e32 v85, 16, v81
	v_and_b32_e32 v81, 0xffff0000, v81
	v_fmac_f32_e32 v87, v84, v84
	v_add_f32_e32 v86, v86, v87
	v_mul_f32_e32 v87, v81, v81
	v_fmac_f32_e32 v87, v85, v85
	v_add_f32_e32 v86, v86, v87
	ds_bpermute_b32 v87, v185, v86
	s_waitcnt lgkmcnt(0)
	v_add_f32_e32 v86, v86, v87
	ds_bpermute_b32 v87, v186, v86
	s_waitcnt lgkmcnt(0)
	v_add_f32_e32 v86, v86, v87
	ds_bpermute_b32 v87, v187, v86
	s_waitcnt lgkmcnt(0)
	v_add_f32_e32 v86, v86, v87
	ds_bpermute_b32 v87, v188, v86
	s_waitcnt lgkmcnt(0)
	v_add_f32_e32 v86, v86, v87
	v_fmamk_f32 v86, v86, 0x3c000000, v167
	v_cmp_gt_f32_e32 vcc, s81, v86
	v_mul_f32_e32 v87, 0x4f800000, v86
	s_nop 0
	v_cndmask_b32_e32 v86, v86, v87, vcc
	v_sqrt_f32_e32 v87, v86
	s_nop 0
	v_add_u32_e32 v88, -1, v87
	v_fma_f32 v89, -v88, v87, v86
	v_cmp_ge_f32_e64 s[72:73], 0, v89
	v_add_u32_e32 v89, 1, v87
	s_nop 0
	v_cndmask_b32_e64 v88, v87, v88, s[72:73]
	v_fma_f32 v87, -v89, v87, v86
	v_cmp_lt_f32_e64 s[72:73], 0, v87
	s_nop 1
	v_cndmask_b32_e64 v87, v88, v89, s[72:73]
	v_mul_f32_e32 v88, 0x37800000, v87
	v_cndmask_b32_e32 v87, v87, v88, vcc
	v_cmp_class_f32_e32 vcc, v86, v168
	s_nop 1
	v_cndmask_b32_e32 v86, v87, v86, vcc
	v_div_scale_f32 v87, s[72:73], v86, v86, 1.0
	v_rcp_f32_e32 v88, v87
	s_nop 0
	v_fma_f32 v89, -v87, v88, 1.0
	v_fmac_f32_e32 v88, v89, v88
	v_div_scale_f32 v89, vcc, 1.0, v86, 1.0
	v_mul_f32_e32 v90, v89, v88
	v_fma_f32 v91, -v87, v90, v89
	v_fmac_f32_e32 v90, v91, v88
	v_fma_f32 v87, -v87, v90, v89
	v_div_fmas_f32 v87, v87, v88, v90
	v_div_fixup_f32 v86, v87, v86, 1.0
	v_mul_f32_e32 v82, v86, v82
	v_mul_f32_e32 v78, v86, v78
	v_mul_f32_e32 v82, v150, v82
	v_mul_f32_e32 v78, v151, v78
	v_cvt_pk_bf16_f32 v78, v82, v78
	v_mul_f32_e32 v82, v86, v83
	v_mul_f32_e32 v79, v86, v79
	v_mul_f32_e32 v82, v152, v82
	v_mul_f32_e32 v79, v153, v79
	v_cvt_pk_bf16_f32 v79, v82, v79
	v_mul_f32_e32 v82, v86, v84
	v_mul_f32_e32 v80, v86, v80
	v_mul_f32_e32 v82, v146, v82
	v_mul_f32_e32 v80, v147, v80
	v_cvt_pk_bf16_f32 v80, v82, v80
	v_mul_f32_e32 v82, v86, v85
	v_mul_f32_e32 v81, v86, v81
	v_mul_f32_e32 v82, v148, v82
	v_mul_f32_e32 v81, v149, v81
	v_cvt_pk_bf16_f32 v81, v82, v81
	v_add_u32_e32 v82, s1, v180
	ds_write_b128 v82, v[66:69]
	v_add_u32_e32 v66, s1, v181
	ds_write_b128 v66, v[70:73]
	v_add_u32_e32 v66, s1, v196
	ds_write_b128 v66, v[74:77] offset:32768
	v_add_u32_e32 v66, s1, v198
	ds_write_b128 v66, v[78:81] offset:32768
	v_mov_b32_e32 v0, v200
	s_waitcnt lgkmcnt(0)
	s_barrier
	s_cbranch_scc1 .LBB0_603
	s_branch .LBB0_469
.LBB0_603:
	s_add_i32 vcc_lo, s95, 7
	s_cmp_lt_u32 vcc_lo, s84
	s_cbranch_scc1 .Lna_skip_last
	s_cmp_ge_u32 vcc_lo, s88
	s_cbranch_scc1 .Lna_skip_last
	v_add_u32_e32 v106, 0, v189
	v_add3_u32 v66, 0, v199, v189
	v_add_u32_e32 v70, v106, v199
	ds_read_b128 v[66:69], v66 offset:49152
	ds_read_b128 v[70:73], v70 offset:57344
	v_add3_u32 v98, 0, v197, v189
	v_add_u32_e32 v102, v106, v197
	ds_read_b128 v[98:101], v98 offset:49152
	ds_read_b128 v[102:105], v102 offset:57344
	s_add_i32 s95, s95, 7
	s_waitcnt lgkmcnt(3)
	v_mfma_f32_32x32x16_bf16 v[82:97], v[66:69], v[114:117], 0
	s_cmp_ge_u32 s95, s84
	s_cselect_b64 s[2:3], -1, 0
	s_cmp_lt_u32 s95, s88
	s_cselect_b64 s[72:73], -1, 0
	s_and_b64 s[72:73], s[2:3], s[72:73]
	s_mov_b64 s[86:87], -1
	s_and_b64 vcc, exec, s[72:73]
	s_waitcnt lgkmcnt(2)
	v_mfma_f32_32x32x16_bf16 v[66:81], v[70:73], v[114:117], 0
	s_waitcnt lgkmcnt(1)
	v_mfma_f32_32x32x16_bf16 v[82:97], v[98:101], v[118:121], v[82:97]
	v_add3_u32 v98, 0, v195, v189
	ds_read_b128 v[98:101], v98 offset:49152
	s_waitcnt lgkmcnt(1)
	v_mfma_f32_32x32x16_bf16 v[66:81], v[102:105], v[118:121], v[66:81]
	v_add_u32_e32 v102, v106, v195
	ds_read_b128 v[102:105], v102 offset:57344
	s_waitcnt lgkmcnt(1)
	v_mfma_f32_32x32x16_bf16 v[82:97], v[98:101], v[122:125], v[82:97]
	v_add3_u32 v98, 0, v194, v189
	ds_read_b128 v[98:101], v98 offset:49152
	s_waitcnt lgkmcnt(1)
	v_mfma_f32_32x32x16_bf16 v[66:81], v[102:105], v[122:125], v[66:81]
	v_add_u32_e32 v102, v106, v194
	ds_read_b128 v[102:105], v102 offset:57344
	s_waitcnt lgkmcnt(1)
	v_mfma_f32_32x32x16_bf16 v[82:97], v[98:101], v[126:129], v[82:97]
	v_add3_u32 v98, 0, v193, v189
	ds_read_b128 v[98:101], v98 offset:49152
	s_waitcnt lgkmcnt(1)
	v_mfma_f32_32x32x16_bf16 v[66:81], v[102:105], v[126:129], v[66:81]
	v_add_u32_e32 v102, v106, v193
	ds_read_b128 v[102:105], v102 offset:57344
	s_waitcnt lgkmcnt(1)
	v_mfma_f32_32x32x16_bf16 v[82:97], v[98:101], v[130:133], v[82:97]
	v_add3_u32 v98, 0, v192, v189
	ds_read_b128 v[98:101], v98 offset:49152
	s_waitcnt lgkmcnt(1)
	v_mfma_f32_32x32x16_bf16 v[66:81], v[102:105], v[130:133], v[66:81]
	v_add_u32_e32 v102, v106, v192
	ds_read_b128 v[102:105], v102 offset:57344
	s_waitcnt lgkmcnt(1)
	v_mfma_f32_32x32x16_bf16 v[82:97], v[98:101], v[134:137], v[82:97]
	v_add3_u32 v98, 0, v191, v189
	ds_read_b128 v[98:101], v98 offset:49152
	s_waitcnt lgkmcnt(1)
	v_mfma_f32_32x32x16_bf16 v[66:81], v[102:105], v[134:137], v[66:81]
	v_add_u32_e32 v102, v106, v191
	ds_read_b128 v[102:105], v102 offset:57344
	s_waitcnt lgkmcnt(1)
	v_mfma_f32_32x32x16_bf16 v[82:97], v[98:101], v[138:141], v[82:97]
	v_add3_u32 v98, 0, v190, v189
	ds_read_b128 v[98:101], v98 offset:49152
	s_waitcnt lgkmcnt(1)
	v_mfma_f32_32x32x16_bf16 v[66:81], v[102:105], v[138:141], v[66:81]
	v_add_u32_e32 v102, v106, v190
	ds_read_b128 v[114:117], v102 offset:57344
	s_waitcnt lgkmcnt(1)
	v_mfma_f32_32x32x16_bf16 v[82:97], v[98:101], v[142:145], v[82:97]
	s_waitcnt lgkmcnt(0)
	v_mfma_f32_32x32x16_bf16 v[66:81], v[114:117], v[142:145], v[66:81]
	s_cbranch_vccnz .LBB0_605
	s_nop 8
	v_mov_b64_e32 v[112:113], v[96:97]
	v_mov_b64_e32 v[98:99], v[82:83]
	v_mov_b64_e32 v[110:111], v[94:95]
	v_mov_b64_e32 v[108:109], v[92:93]
	v_mov_b64_e32 v[106:107], v[90:91]
	v_mov_b64_e32 v[104:105], v[88:89]
	v_mov_b64_e32 v[102:103], v[86:87]
	v_mov_b64_e32 v[100:101], v[84:85]
	v_mov_b32_e32 v98, s80
	s_mov_b64 s[86:87], 0

.Lna_skip_last:
	v_readlane_b32 s96, v252, 26
	v_readlane_b32 s97, v252, 27
	v_readlane_b32 s64, v252, 7
	v_readlane_b32 s65, v252, 8
	s_barrier
	s_and_saveexec_b64 s[6:7], s[4:5]
	ds_write_b32 v179, v0
	s_branch .LBB0_463
